# merged-GEMM epilogue gate loads batched 8 at a time; P0 w_in column-max pass issues its 16 loads together; P8 slot position/weight loads issued with the expert-id load
# baseline (speedup 1.0000x reference)
; __device__ __forceinline__ float shx(float v, int mask, int lane) { return __int_as_float(__builtin_amdgcn_ds_bpermute((lane ^ mask) << 2, __float_as_int(v))); }
; __device__ __forceinline__ void win_pass1(const Params& p, int l, int job, int lane) {
;     const int kb = job / 96, cb = job % 96; const int kr = lane >> 4, n4 = (lane & 15) * 4;
;     const float* sp = p.in[3] + (size_t)l * D * INC + (size_t)(kb * 64) * INC + cb * 64;
;     f32x4 am = (f32x4){0.f, 0.f, 0.f, 0.f};
; #pragma unroll
;     for (int q = 0; q < 16; ++q) { const f32x4 x = *(const f32x4*)(sp + (size_t)(4 * q + kr) * INC + n4);
;         am.x = fmaxf(am.x, fabsf(x.x)); am.y = fmaxf(am.y, fabsf(x.y)); am.z = fmaxf(am.z, fabsf(x.z)); am.w = fmaxf(am.w, fabsf(x.w)); }
;     am.x = fmaxf(am.x, shx(am.x, 16, lane)); am.y = fmaxf(am.y, shx(am.y, 16, lane)); am.z = fmaxf(am.z, shx(am.z, 16, lane)); am.w = fmaxf(am.w, shx(am.w, 16, lane));
;     am.x = fmaxf(am.x, shx(am.x, 32, lane)); am.y = fmaxf(am.y, shx(am.y, 32, lane)); am.z = fmaxf(am.z, shx(am.z, 32, lane)); am.w = fmaxf(am.w, shx(am.w, 32, lane));
;     unsigned* ctl = (unsigned*)(p.ws + WS_CTL);
;     unsigned dep = 0u;
;     if (lane < 16) { unsigned* cm = ctl + CW_CMAX + l * INC + cb * 64 + n4;
;         dep = __hip_atomic_fetch_max(cm, __float_as_uint(am.x), __ATOMIC_RELAXED, __HIP_MEMORY_SCOPE_AGENT) | __hip_atomic_fetch_max(cm + 1, __float_as_uint(am.y), __ATOMIC_RELAXED, __HIP_MEMORY_SCOPE_AGENT)
;             | __hip_atomic_fetch_max(cm + 2, __float_as_uint(am.z), __ATOMIC_RELAXED, __HIP_MEMORY_SCOPE_AGENT) | __hip_atomic_fetch_max(cm + 3, __float_as_uint(am.w), __ATOMIC_RELAXED, __HIP_MEMORY_SCOPE_AGENT); }
;     asm volatile("s_waitcnt vmcnt(0)" : "+v"(dep) :: "memory");
;     dep = (unsigned)__builtin_amdgcn_readfirstlane((int)dep) & 0u;
.LBB0_13:
	s_mul_hi_i32 s2, s71, 0x2aaaaaab
	s_lshr_b32 s3, s2, 31
	s_ashr_i32 s43, s2, 9
	s_add_i32 s43, s43, s3
	s_mul_i32 s2, s43, 0xfffff400
	s_add_i32 s2, s71, s2
	s_mul_i32 s3, s2, 0x2aab
	s_lshr_b32 s42, s3, 31
	s_ashr_i32 s3, s3, 20
	s_add_i32 s3, s3, s42
	s_mul_i32 s42, s3, 0x60
	s_sub_i32 s2, s2, s42
	s_mul_i32 s44, s43, 0x3000000
	s_sext_i32_i16 s42, s2
	s_mul_hi_i32 s2, s43, 0x3000000
	s_add_u32 s44, s10, s44
	s_addc_u32 s2, s11, s2
	s_mul_hi_i32 s45, s3, 0x180000
	s_mul_i32 s3, s3, 0x180000
	s_add_u32 s46, s44, s3
	s_addc_u32 s47, s2, s45
	s_lshl_b32 s2, s42, 6
	s_ashr_i32 s3, s2, 31
	s_lshl_b64 s[44:45], s[2:3], 2
	s_add_u32 s2, s46, s44
	s_addc_u32 s3, s47, s45
	v_lshl_add_u64 v[8:9], s[2:3], 0, v[2:3]
	v_lshl_add_u64 v[64:65], v[8:9], 0, v[4:5]
	s_waitcnt lgkmcnt(0)
	v_mov_b64_e32 v[72:73], v[64:65]
	s_mov_b64 s[2:3], 0x18000
	global_load_dwordx4 v[8:11], v[72:73], off
	v_lshl_add_u64 v[72:73], v[72:73], 0, s[2:3]
	global_load_dwordx4 v[12:15], v[72:73], off
	v_lshl_add_u64 v[72:73], v[72:73], 0, s[2:3]
	global_load_dwordx4 v[16:19], v[72:73], off
	v_lshl_add_u64 v[72:73], v[72:73], 0, s[2:3]
	global_load_dwordx4 v[20:23], v[72:73], off
	v_lshl_add_u64 v[72:73], v[72:73], 0, s[2:3]
	global_load_dwordx4 v[24:27], v[72:73], off
	v_lshl_add_u64 v[72:73], v[72:73], 0, s[2:3]
	global_load_dwordx4 v[28:31], v[72:73], off
	v_lshl_add_u64 v[72:73], v[72:73], 0, s[2:3]
	global_load_dwordx4 v[32:35], v[72:73], off
	v_lshl_add_u64 v[72:73], v[72:73], 0, s[2:3]
	global_load_dwordx4 v[36:39], v[72:73], off
	v_lshl_add_u64 v[72:73], v[72:73], 0, s[2:3]
	global_load_dwordx4 v[40:43], v[72:73], off
	v_lshl_add_u64 v[72:73], v[72:73], 0, s[2:3]
	global_load_dwordx4 v[44:47], v[72:73], off
	v_lshl_add_u64 v[72:73], v[72:73], 0, s[2:3]
	global_load_dwordx4 v[48:51], v[72:73], off
	v_lshl_add_u64 v[72:73], v[72:73], 0, s[2:3]
	global_load_dwordx4 v[52:55], v[72:73], off
	v_lshl_add_u64 v[72:73], v[72:73], 0, s[2:3]
	global_load_dwordx4 v[56:59], v[72:73], off
	v_lshl_add_u64 v[72:73], v[72:73], 0, s[2:3]
	global_load_dwordx4 v[60:63], v[72:73], off
	v_lshl_add_u64 v[72:73], v[72:73], 0, s[2:3]
	global_load_dwordx4 v[64:67], v[72:73], off
	v_lshl_add_u64 v[72:73], v[72:73], 0, s[2:3]
	global_load_dwordx4 v[68:71], v[72:73], off
	s_waitcnt vmcnt(14)
	v_max3_f32 v82, |v8|, 0, |v12|
	v_max3_f32 v83, |v9|, 0, |v13|
	v_max3_f32 v84, |v10|, 0, |v14|
	v_max3_f32 v85, |v11|, 0, |v15|
	s_waitcnt vmcnt(12)
	v_max3_f32 v82, v82, |v16|, |v20|
	v_max3_f32 v83, v83, |v17|, |v21|
	v_max3_f32 v84, v84, |v18|, |v22|
	v_max3_f32 v85, v85, |v19|, |v23|
	s_waitcnt vmcnt(10)
	v_max3_f32 v82, v82, |v24|, |v28|
	v_max3_f32 v83, v83, |v25|, |v29|
	v_max3_f32 v84, v84, |v26|, |v30|
	v_max3_f32 v85, v85, |v27|, |v31|
	s_waitcnt vmcnt(8)
	v_max3_f32 v82, v82, |v32|, |v36|
	v_max3_f32 v83, v83, |v33|, |v37|
	v_max3_f32 v84, v84, |v34|, |v38|
	v_max3_f32 v85, v85, |v35|, |v39|
	s_waitcnt vmcnt(6)
	v_max3_f32 v82, v82, |v40|, |v44|
	v_max3_f32 v83, v83, |v41|, |v45|
	v_max3_f32 v84, v84, |v42|, |v46|
	v_max3_f32 v85, v85, |v43|, |v47|
	s_waitcnt vmcnt(4)
	v_max3_f32 v82, v82, |v48|, |v52|
	v_max3_f32 v83, v83, |v49|, |v53|
	v_max3_f32 v84, v84, |v50|, |v54|
	v_max3_f32 v85, v85, |v51|, |v55|
	s_waitcnt vmcnt(2)
	v_max3_f32 v82, v82, |v56|, |v60|
	v_max3_f32 v83, v83, |v57|, |v61|
	v_max3_f32 v84, v84, |v58|, |v62|
	v_max3_f32 v85, v85, |v59|, |v63|
	s_waitcnt vmcnt(0)
	v_max3_f32 v82, v82, |v64|, |v68|
	v_max3_f32 v83, v83, |v65|, |v69|
	v_max3_f32 v84, v84, |v66|, |v70|
	v_max3_f32 v85, v85, |v67|, |v71|
	v_mov_b32_e32 v8, v82
	v_mov_b32_e32 v9, v83
	v_mov_b32_e32 v10, v84
	v_mov_b32_e32 v13, v85
	v_mov_b32_e32 v15, 0
	ds_bpermute_b32 v12, v6, v8
	ds_bpermute_b32 v11, v6, v9
	s_waitcnt lgkmcnt(0)
	v_max_f32_e32 v12, v12, v12
	ds_bpermute_b32 v14, v6, v10
	v_max_f32_e32 v8, v8, v12
	ds_bpermute_b32 v12, v6, v13
	v_max_f32_e32 v11, v11, v11
	v_max_f32_e32 v9, v9, v11
	s_waitcnt lgkmcnt(1)
	v_max_f32_e32 v11, v14, v14
	v_max_f32_e32 v11, v10, v11
	s_waitcnt lgkmcnt(0)
	v_max_f32_e32 v10, v12, v12
	v_max_f32_e32 v13, v13, v10
	ds_bpermute_b32 v10, v7, v8
	ds_bpermute_b32 v12, v7, v9
	ds_bpermute_b32 v14, v7, v11
	ds_bpermute_b32 v16, v7, v13
	s_and_saveexec_b64 s[2:3], s[0:1]
	s_cbranch_execz .LBB0_15
	s_mul_i32 s46, s43, 0x1800
	s_ashr_i32 s47, s46, 31
	s_lshl_b64 s[46:47], s[46:47], 2
	s_add_u32 s46, s56, s46
	s_addc_u32 s47, s57, s47
	s_waitcnt lgkmcnt(1)
	v_max_f32_e32 v14, v14, v14
	v_max_f32_e32 v11, v11, v11
	v_max_f32_e32 v12, v12, v12
	v_max_f32_e32 v9, v9, v9
	v_max_f32_e32 v10, v10, v10
	v_max_f32_e32 v8, v8, v8
	s_add_u32 s44, s46, s44
	s_waitcnt lgkmcnt(0)
	v_max_f32_e32 v15, v16, v16
	v_max_f32_e32 v13, v13, v13
	v_max_f32_e32 v11, v11, v14
	v_max_f32_e32 v9, v9, v12
	v_max_f32_e32 v8, v8, v10
	s_addc_u32 s45, s47, s45
	v_max_f32_e32 v13, v13, v15
	global_atomic_umax v8, v2, v8, s[44:45] sc0
	s_nop 0
	global_atomic_umax v9, v2, v9, s[44:45] offset:4 sc0
	s_nop 0
	global_atomic_umax v10, v2, v11, s[44:45] offset:8 sc0
	s_nop 0
	global_atomic_umax v11, v2, v13, s[44:45] offset:12 sc0
	s_waitcnt vmcnt(2)
	v_or_b32_e32 v8, v9, v8
	s_waitcnt vmcnt(0)
	v_or3_b32 v15, v8, v10, v11

; __device__ __forceinline__ float bflo(unsigned w) { return __uint_as_float(w << 16); }
; __device__ __forceinline__ float bfhi(unsigned w) { return __uint_as_float(w & 0xffff0000u); }
; __device__ __forceinline__ unsigned pk4_fp8(float a, float b, float c, float d) { unsigned w = 0u; w = __builtin_amdgcn_cvt_pk_fp8_f32(clamp8(a), clamp8(b), w, false); w = __builtin_amdgcn_cvt_pk_fp8_f32(clamp8(c), clamp8(d), w, true); return w; }
;     __device__ __forceinline__ void operator()(const f32x4 (&acc)[2][2][4][2], const Unit& u, int wr, int wc, int fr, int fq) const {
;     ...
;             for (int m = 0; m < 4; ++m) { const size_t r = (size_t)(row0 + ai * HALF + m * 16);
; #pragma unroll
;                 for (int bj = 0; bj < 2; ++bj) { const int col = u.pn * BM + bj * HALF + colw;
;                     const u32x4 gw = *(const u32x4*)(GATE + r * INC + 2 * D + col);
;                     f32x4 r0 = acc[ai][bj][m][0], r1 = acc[ai][bj][m][1];
;                     r0[0] *= bflo(gw.x); r0[1] *= bfhi(gw.x); r0[2] *= bflo(gw.y); r0[3] *= bfhi(gw.y); r1[0] *= bflo(gw.z); r1[1] *= bfhi(gw.z); r1[2] *= bflo(gw.w); r1[3] *= bfhi(gw.w);
;                     u32x2 w; w.x = pk4_fp8(4.f * r0[0], 4.f * r0[1], 4.f * r0[2], 4.f * r0[3]); w.y = pk4_fp8(4.f * r1[0], 4.f * r1[1], 4.f * r1[2], 4.f * r1[3]); *(u32x2*)(MG + r * D + col) = w; }
;                 asm volatile("" ::: "memory"); }
.LBB0_722:
	v_readlane_b32 s6, v251, 3
	v_readlane_b32 s7, v251, 4
	v_or_b32_e32 v0, s12, v206
	s_mov_b64 s[10:11], 0x2000
	v_mov_b64_e32 v[2:3], s[6:7]
	v_mad_i64_i32 v[4:5], s[6:7], v212, s97, v[2:3]
	v_ashrrev_i32_e32 v1, 31, v0
	v_lshl_add_u64 v[8:9], v[4:5], 0, s[10:11]
	v_lshlrev_b64 v[4:5], 1, v[0:1]
	v_mad_i64_i32 v[52:53], s[6:7], v212, s97, v[2:3]
	v_lshl_add_u64 v[52:53], v[52:53], 0, s[10:11]
	v_lshl_add_u64 v[52:53], v[52:53], 0, v[4:5]
	global_load_dwordx4 v[20:23], v[52:53], off
	global_load_dwordx4 v[24:27], v[52:53], off offset:256
	v_add_u32_e32 v52, 16, v212
	v_mad_i64_i32 v[52:53], s[6:7], v52, s97, v[2:3]
	v_lshl_add_u64 v[52:53], v[52:53], 0, s[10:11]
	v_lshl_add_u64 v[52:53], v[52:53], 0, v[4:5]
	global_load_dwordx4 v[28:31], v[52:53], off
	global_load_dwordx4 v[32:35], v[52:53], off offset:256
	v_add_u32_e32 v52, 32, v212
	v_mad_i64_i32 v[52:53], s[6:7], v52, s97, v[2:3]
	v_lshl_add_u64 v[52:53], v[52:53], 0, s[10:11]
	v_lshl_add_u64 v[52:53], v[52:53], 0, v[4:5]
	global_load_dwordx4 v[36:39], v[52:53], off
	global_load_dwordx4 v[40:43], v[52:53], off offset:256
	v_add_u32_e32 v52, 48, v212
	v_mad_i64_i32 v[52:53], s[6:7], v52, s97, v[2:3]
	v_lshl_add_u64 v[52:53], v[52:53], 0, s[10:11]
	v_lshl_add_u64 v[52:53], v[52:53], 0, v[4:5]
	global_load_dwordx4 v[44:47], v[52:53], off
	global_load_dwordx4 v[48:51], v[52:53], off offset:256
	v_lshl_add_u64 v[10:11], v[8:9], 0, v[4:5]
	s_waitcnt vmcnt(7)
	v_mov_b64_e32 v[10:11], v[20:21]
	v_mov_b64_e32 v[12:13], v[22:23]
	v_ashrrev_i32_e32 v213, 31, v212
	v_readlane_b32 s8, v252, 20
	v_lshlrev_b64 v[6:7], 11, v[212:213]
	v_readlane_b32 s9, v252, 21
	s_and_b64 vcc, exec, s[0:1]
	s_mov_b64 s[0:1], -1
	v_lshl_add_u64 v[6:7], s[8:9], 0, v[6:7]
	v_lshlrev_b32_e32 v16, 16, v12
	v_and_b32_e32 v12, 0xffff0000, v12
	v_lshlrev_b32_e32 v14, 16, v10
	v_and_b32_e32 v10, 0xffff0000, v10
	v_mul_f32_e32 v17, v187, v12
	v_lshlrev_b32_e32 v12, 16, v13
	v_mul_f32_e32 v14, v190, v14
	v_mul_f32_e32 v10, v191, v10
	v_lshlrev_b32_e32 v15, 16, v11
	v_mul_f32_e32 v18, v188, v12
	v_and_b32_e32 v12, 0xffff0000, v13
	v_mul_f32_e32 v15, v192, v15
	v_mul_f32_e32 v13, v189, v12
	v_mul_f32_e32 v12, 4.0, v14
	v_mul_f32_e32 v10, 4.0, v10
	v_mul_f32_e32 v14, 4.0, v15
	v_med3_f32 v15, v12, s33, v229
	v_med3_f32 v10, v10, s33, v229
	v_mov_b32_e32 v12, v65
	v_and_b32_e32 v11, 0xffff0000, v11
	v_cvt_pk_fp8_f32 v12, v15, v10
	v_mul_f32_e32 v11, v193, v11
	v_mul_f32_e32 v11, 4.0, v11
	v_mul_f32_e32 v16, v186, v16
	v_med3_f32 v10, v14, s33, v229
	v_med3_f32 v11, v11, s33, v229
	v_cvt_pk_fp8_f32 v12, v10, v11 op_sel:[0,0,1]
	v_mul_f32_e32 v10, 4.0, v16
	v_mul_f32_e32 v11, 4.0, v17
	v_mul_f32_e32 v15, 4.0, v13
	v_med3_f32 v10, v10, s33, v229
	v_med3_f32 v11, v11, s33, v229
	v_mov_b32_e32 v13, v65
	v_cvt_pk_fp8_f32 v13, v10, v11
	v_mul_f32_e32 v14, 4.0, v18
	v_med3_f32 v10, v14, s33, v229
	v_med3_f32 v11, v15, s33, v229
	v_cvt_pk_fp8_f32 v13, v10, v11 op_sel:[0,0,1]
	v_lshl_add_u64 v[10:11], v[6:7], 0, v[0:1]
	v_or_b32_e32 v6, 0x80, v0
	v_ashrrev_i32_e32 v7, 31, v6
	v_lshlrev_b64 v[6:7], 1, v[6:7]
	global_store_dwordx2 v[10:11], v[12:13], off
	v_lshl_add_u64 v[8:9], v[8:9], 0, v[6:7]
	s_waitcnt vmcnt(7)
	v_mov_b64_e32 v[12:13], v[24:25]
	v_mov_b64_e32 v[14:15], v[26:27]
	v_lshlrev_b32_e32 v8, 16, v12
	v_and_b32_e32 v9, 0xffff0000, v12
	v_mul_f32_e32 v8, v182, v8
	v_mul_f32_e32 v9, v183, v9
	v_mul_f32_e32 v8, 4.0, v8
	v_mul_f32_e32 v9, 4.0, v9
	v_med3_f32 v18, v8, s33, v229
	v_med3_f32 v9, v9, s33, v229
	v_mov_b32_e32 v8, v65
	v_lshlrev_b32_e32 v12, 16, v13
	v_and_b32_e32 v13, 0xffff0000, v13
	v_cvt_pk_fp8_f32 v8, v18, v9
	v_mul_f32_e32 v12, v184, v12
	v_mul_f32_e32 v13, v185, v13
	v_lshlrev_b32_e32 v16, 16, v14
	v_and_b32_e32 v14, 0xffff0000, v14
	v_mul_f32_e32 v12, 4.0, v12
	v_mul_f32_e32 v13, 4.0, v13
	v_mul_f32_e32 v16, v178, v16
	v_mul_f32_e32 v14, v179, v14
	v_lshlrev_b32_e32 v17, 16, v15
	v_and_b32_e32 v15, 0xffff0000, v15
	v_med3_f32 v9, v12, s33, v229
	v_med3_f32 v12, v13, s33, v229
	v_mul_f32_e32 v15, v181, v15
	v_cvt_pk_fp8_f32 v8, v9, v12 op_sel:[0,0,1]
	v_mul_f32_e32 v9, 4.0, v16
	v_mul_f32_e32 v12, 4.0, v14
	v_mul_f32_e32 v14, 4.0, v15
	v_med3_f32 v15, v9, s33, v229
	v_med3_f32 v12, v12, s33, v229
	v_mov_b32_e32 v9, v65
	v_cvt_pk_fp8_f32 v9, v15, v12
	v_mul_f32_e32 v17, v180, v17
	v_mul_f32_e32 v13, 4.0, v17
	v_med3_f32 v12, v13, s33, v229
	v_med3_f32 v13, v14, s33, v229
	v_cvt_pk_fp8_f32 v9, v12, v13 op_sel:[0,0,1]
	global_store_dwordx2 v[10:11], v[8:9], off offset:128
	v_add_u32_e32 v10, 16, v212
	v_ashrrev_i32_e32 v11, 31, v10
	v_lshlrev_b64 v[8:9], 11, v[10:11]
	v_mad_i64_i32 v[10:11], s[6:7], v10, s97, v[2:3]
	v_lshl_add_u64 v[10:11], v[10:11], 0, s[10:11]
	v_lshl_add_u64 v[12:13], v[10:11], 0, v[4:5]
	s_waitcnt vmcnt(7)
	v_mov_b64_e32 v[12:13], v[28:29]
	v_mov_b64_e32 v[14:15], v[30:31]
	v_lshl_add_u64 v[8:9], s[8:9], 0, v[8:9]
	v_lshlrev_b32_e32 v16, 16, v12
	v_and_b32_e32 v12, 0xffff0000, v12
	v_mul_f32_e32 v16, v174, v16
	v_mul_f32_e32 v12, v175, v12
	v_mul_f32_e32 v16, 4.0, v16
	v_mul_f32_e32 v12, 4.0, v12
	v_med3_f32 v16, v16, s33, v229
	v_med3_f32 v20, v12, s33, v229
	v_mov_b32_e32 v12, v65
	v_lshlrev_b32_e32 v17, 16, v13
	v_and_b32_e32 v13, 0xffff0000, v13
	v_cvt_pk_fp8_f32 v12, v16, v20
	v_mul_f32_e32 v17, v176, v17
	v_mul_f32_e32 v13, v177, v13
	v_lshlrev_b32_e32 v18, 16, v14
	v_and_b32_e32 v14, 0xffff0000, v14
	v_mul_f32_e32 v17, 4.0, v17
	v_mul_f32_e32 v13, 4.0, v13
	v_mul_f32_e32 v18, v170, v18
	v_mul_f32_e32 v14, v171, v14
	v_med3_f32 v16, v17, s33, v229
	v_med3_f32 v13, v13, s33, v229
	v_cvt_pk_fp8_f32 v12, v16, v13 op_sel:[0,0,1]
	v_mul_f32_e32 v13, 4.0, v18
	v_mul_f32_e32 v14, 4.0, v14
	v_med3_f32 v17, v13, s33, v229
	v_med3_f32 v14, v14, s33, v229
	v_mov_b32_e32 v13, v65
	v_lshlrev_b32_e32 v19, 16, v15
	v_and_b32_e32 v15, 0xffff0000, v15
	v_cvt_pk_fp8_f32 v13, v17, v14
	v_mul_f32_e32 v19, v172, v19
	v_mul_f32_e32 v15, v173, v15
	v_mul_f32_e32 v16, 4.0, v19
	v_mul_f32_e32 v15, 4.0, v15
	v_med3_f32 v14, v16, s33, v229
	v_med3_f32 v15, v15, s33, v229
	v_cvt_pk_fp8_f32 v13, v14, v15 op_sel:[0,0,1]
	v_lshl_add_u64 v[14:15], v[8:9], 0, v[0:1]
	v_lshl_add_u64 v[8:9], v[10:11], 0, v[6:7]
	global_store_dwordx2 v[14:15], v[12:13], off
	s_waitcnt vmcnt(7)
; __device__ __forceinline__ float bflo(unsigned w) { return __uint_as_float(w << 16); }
; __device__ __forceinline__ float bfhi(unsigned w) { return __uint_as_float(w & 0xffff0000u); }
; __device__ __forceinline__ unsigned pk4_fp8(float a, float b, float c, float d) { unsigned w = 0u; w = __builtin_amdgcn_cvt_pk_fp8_f32(clamp8(a), clamp8(b), w, false); w = __builtin_amdgcn_cvt_pk_fp8_f32(clamp8(c), clamp8(d), w, true); return w; }
;     __device__ __forceinline__ void operator()(const f32x4 (&acc)[2][2][4][2], const Unit& u, int wr, int wc, int fr, int fq) const {
;     ...
;             for (int m = 0; m < 4; ++m) { const size_t r = (size_t)(row0 + ai * HALF + m * 16);
; #pragma unroll
;                 for (int bj = 0; bj < 2; ++bj) { const int col = u.pn * BM + bj * HALF + colw;
;                     const u32x4 gw = *(const u32x4*)(GATE + r * INC + 2 * D + col);
;                     f32x4 r0 = acc[ai][bj][m][0], r1 = acc[ai][bj][m][1];
;                     r0[0] *= bflo(gw.x); r0[1] *= bfhi(gw.x); r0[2] *= bflo(gw.y); r0[3] *= bfhi(gw.y); r1[0] *= bflo(gw.z); r1[1] *= bfhi(gw.z); r1[2] *= bflo(gw.w); r1[3] *= bfhi(gw.w);
;                     u32x2 w; w.x = pk4_fp8(4.f * r0[0], 4.f * r0[1], 4.f * r0[2], 4.f * r0[3]); w.y = pk4_fp8(4.f * r1[0], 4.f * r1[1], 4.f * r1[2], 4.f * r1[3]); *(u32x2*)(MG + r * D + col) = w; }
;                 asm volatile("" ::: "memory"); }
	v_mov_b64_e32 v[8:9], v[32:33]
	v_mov_b64_e32 v[10:11], v[34:35]
	v_lshlrev_b32_e32 v12, 16, v8
	v_and_b32_e32 v8, 0xffff0000, v8
	v_mul_f32_e32 v12, v166, v12
	v_mul_f32_e32 v8, v167, v8
	v_mul_f32_e32 v12, 4.0, v12
	v_mul_f32_e32 v8, 4.0, v8
	v_med3_f32 v12, v12, s33, v229
	v_med3_f32 v18, v8, s33, v229
	v_mov_b32_e32 v8, v65
	v_lshlrev_b32_e32 v13, 16, v9
	v_and_b32_e32 v9, 0xffff0000, v9
	v_cvt_pk_fp8_f32 v8, v12, v18
	v_mul_f32_e32 v13, v168, v13
	v_mul_f32_e32 v9, v169, v9
	v_lshlrev_b32_e32 v16, 16, v10
	v_and_b32_e32 v10, 0xffff0000, v10
	v_mul_f32_e32 v13, 4.0, v13
	v_mul_f32_e32 v9, 4.0, v9
	v_mul_f32_e32 v16, v162, v16
	v_mul_f32_e32 v10, v163, v10
	v_med3_f32 v12, v13, s33, v229
	v_med3_f32 v9, v9, s33, v229
	v_cvt_pk_fp8_f32 v8, v12, v9 op_sel:[0,0,1]
	v_mul_f32_e32 v9, 4.0, v16
	v_mul_f32_e32 v10, 4.0, v10
	v_med3_f32 v13, v9, s33, v229
	v_med3_f32 v10, v10, s33, v229
	v_mov_b32_e32 v9, v65
	v_lshlrev_b32_e32 v17, 16, v11
	v_and_b32_e32 v11, 0xffff0000, v11
	v_cvt_pk_fp8_f32 v9, v13, v10
	v_mul_f32_e32 v17, v164, v17
	v_mul_f32_e32 v11, v165, v11
	v_mul_f32_e32 v12, 4.0, v17
	v_mul_f32_e32 v11, 4.0, v11
	v_med3_f32 v10, v12, s33, v229
	v_med3_f32 v11, v11, s33, v229
	v_cvt_pk_fp8_f32 v9, v10, v11 op_sel:[0,0,1]
	v_add_u32_e32 v10, 32, v212
	v_ashrrev_i32_e32 v11, 31, v10
	global_store_dwordx2 v[14:15], v[8:9], off offset:128
	v_lshlrev_b64 v[8:9], 11, v[10:11]
	v_mad_i64_i32 v[10:11], s[6:7], v10, s97, v[2:3]
	v_lshl_add_u64 v[10:11], v[10:11], 0, s[10:11]
	v_lshl_add_u64 v[12:13], v[10:11], 0, v[4:5]
	s_waitcnt vmcnt(7)
	v_mov_b64_e32 v[12:13], v[36:37]
	v_mov_b64_e32 v[14:15], v[38:39]
	v_lshl_add_u64 v[8:9], s[8:9], 0, v[8:9]
	v_lshlrev_b32_e32 v16, 16, v12
	v_and_b32_e32 v12, 0xffff0000, v12
	v_mul_f32_e32 v16, v158, v16
	v_mul_f32_e32 v12, v159, v12
	v_mul_f32_e32 v16, 4.0, v16
	v_mul_f32_e32 v12, 4.0, v12
	v_med3_f32 v16, v16, s33, v229
	v_med3_f32 v20, v12, s33, v229
	v_mov_b32_e32 v12, v65
	v_lshlrev_b32_e32 v17, 16, v13
	v_and_b32_e32 v13, 0xffff0000, v13
	v_cvt_pk_fp8_f32 v12, v16, v20
	v_mul_f32_e32 v17, v160, v17
	v_mul_f32_e32 v13, v161, v13
	v_lshlrev_b32_e32 v18, 16, v14
	v_and_b32_e32 v14, 0xffff0000, v14
	v_mul_f32_e32 v17, 4.0, v17
	v_mul_f32_e32 v13, 4.0, v13
	v_mul_f32_e32 v18, v154, v18
	v_mul_f32_e32 v14, v155, v14
	v_med3_f32 v16, v17, s33, v229
	v_med3_f32 v13, v13, s33, v229
	v_cvt_pk_fp8_f32 v12, v16, v13 op_sel:[0,0,1]
	v_mul_f32_e32 v13, 4.0, v18
	v_mul_f32_e32 v14, 4.0, v14
	v_med3_f32 v17, v13, s33, v229
	v_med3_f32 v14, v14, s33, v229
	v_mov_b32_e32 v13, v65
	v_lshlrev_b32_e32 v19, 16, v15
	v_and_b32_e32 v15, 0xffff0000, v15
	v_cvt_pk_fp8_f32 v13, v17, v14
	v_mul_f32_e32 v19, v156, v19
	v_mul_f32_e32 v15, v157, v15
	v_mul_f32_e32 v16, 4.0, v19
	v_mul_f32_e32 v15, 4.0, v15
	v_med3_f32 v14, v16, s33, v229
	v_med3_f32 v15, v15, s33, v229
	v_cvt_pk_fp8_f32 v13, v14, v15 op_sel:[0,0,1]
	v_lshl_add_u64 v[14:15], v[8:9], 0, v[0:1]
	v_lshl_add_u64 v[8:9], v[10:11], 0, v[6:7]
	global_store_dwordx2 v[14:15], v[12:13], off
	s_waitcnt vmcnt(7)
	v_mov_b64_e32 v[8:9], v[40:41]
	v_mov_b64_e32 v[10:11], v[42:43]
	v_lshlrev_b32_e32 v12, 16, v8
	v_and_b32_e32 v8, 0xffff0000, v8
	v_mul_f32_e32 v12, v150, v12
	v_mul_f32_e32 v8, v151, v8
	v_mul_f32_e32 v12, 4.0, v12
	v_mul_f32_e32 v8, 4.0, v8
	v_med3_f32 v12, v12, s33, v229
	v_med3_f32 v18, v8, s33, v229
	v_mov_b32_e32 v8, v65
	v_lshlrev_b32_e32 v13, 16, v9
	v_and_b32_e32 v9, 0xffff0000, v9
	v_cvt_pk_fp8_f32 v8, v12, v18
	v_mul_f32_e32 v13, v152, v13
	v_mul_f32_e32 v9, v153, v9
	v_lshlrev_b32_e32 v16, 16, v10
	v_and_b32_e32 v10, 0xffff0000, v10
	v_mul_f32_e32 v13, 4.0, v13
	v_mul_f32_e32 v9, 4.0, v9
	v_mul_f32_e32 v16, v146, v16
	v_mul_f32_e32 v10, v147, v10
	v_med3_f32 v12, v13, s33, v229
	v_med3_f32 v9, v9, s33, v229
	v_cvt_pk_fp8_f32 v8, v12, v9 op_sel:[0,0,1]
	v_mul_f32_e32 v9, 4.0, v16
	v_mul_f32_e32 v10, 4.0, v10
	v_med3_f32 v13, v9, s33, v229
	v_med3_f32 v10, v10, s33, v229
	v_mov_b32_e32 v9, v65
	v_lshlrev_b32_e32 v17, 16, v11
	v_and_b32_e32 v11, 0xffff0000, v11
	v_cvt_pk_fp8_f32 v9, v13, v10
	v_mul_f32_e32 v17, v148, v17
	v_mul_f32_e32 v11, v149, v11
	v_mul_f32_e32 v12, 4.0, v17
	v_mul_f32_e32 v11, 4.0, v11
	v_med3_f32 v10, v12, s33, v229
	v_med3_f32 v11, v11, s33, v229
	v_cvt_pk_fp8_f32 v9, v10, v11 op_sel:[0,0,1]
	v_add_u32_e32 v10, 48, v212
	v_ashrrev_i32_e32 v11, 31, v10
	global_store_dwordx2 v[14:15], v[8:9], off offset:128
	v_lshlrev_b64 v[8:9], 11, v[10:11]
	v_mad_i64_i32 v[10:11], s[6:7], v10, s97, v[2:3]
	v_lshl_add_u64 v[10:11], v[10:11], 0, s[10:11]
	v_lshl_add_u64 v[12:13], v[10:11], 0, v[4:5]
	s_waitcnt vmcnt(7)
	v_mov_b64_e32 v[12:13], v[44:45]
	v_mov_b64_e32 v[14:15], v[46:47]
	v_lshl_add_u64 v[8:9], s[8:9], 0, v[8:9]
	v_lshlrev_b32_e32 v16, 16, v12
	v_and_b32_e32 v12, 0xffff0000, v12
	v_mul_f32_e32 v16, v142, v16
	v_mul_f32_e32 v12, v143, v12
	v_mul_f32_e32 v16, 4.0, v16
	v_mul_f32_e32 v12, 4.0, v12
	v_med3_f32 v16, v16, s33, v229
	v_med3_f32 v20, v12, s33, v229
	v_mov_b32_e32 v12, v65
	v_lshlrev_b32_e32 v17, 16, v13
	v_and_b32_e32 v13, 0xffff0000, v13
	v_cvt_pk_fp8_f32 v12, v16, v20
	v_mul_f32_e32 v17, v144, v17
	v_mul_f32_e32 v13, v145, v13
	v_lshlrev_b32_e32 v18, 16, v14
	v_and_b32_e32 v14, 0xffff0000, v14
	v_mul_f32_e32 v17, 4.0, v17
	v_mul_f32_e32 v13, 4.0, v13
	v_mul_f32_e32 v18, v138, v18
	v_mul_f32_e32 v14, v139, v14
	v_med3_f32 v16, v17, s33, v229
	v_med3_f32 v13, v13, s33, v229
	v_cvt_pk_fp8_f32 v12, v16, v13 op_sel:[0,0,1]
	v_mul_f32_e32 v13, 4.0, v18
	v_mul_f32_e32 v14, 4.0, v14
	v_med3_f32 v17, v13, s33, v229
	v_med3_f32 v14, v14, s33, v229
	v_mov_b32_e32 v13, v65
	v_lshlrev_b32_e32 v19, 16, v15
	v_and_b32_e32 v15, 0xffff0000, v15
	v_cvt_pk_fp8_f32 v13, v17, v14
	v_mul_f32_e32 v19, v140, v19
	v_mul_f32_e32 v15, v141, v15
	v_mul_f32_e32 v16, 4.0, v19
	v_mul_f32_e32 v15, 4.0, v15
	v_med3_f32 v14, v16, s33, v229
	v_med3_f32 v15, v15, s33, v229
	v_cvt_pk_fp8_f32 v13, v14, v15 op_sel:[0,0,1]
	v_lshl_add_u64 v[14:15], v[8:9], 0, v[0:1]
	v_lshl_add_u64 v[8:9], v[10:11], 0, v[6:7]
	global_store_dwordx2 v[14:15], v[12:13], off
	s_waitcnt vmcnt(7)
; __device__ __forceinline__ float bflo(unsigned w) { return __uint_as_float(w << 16); }
; __device__ __forceinline__ float bfhi(unsigned w) { return __uint_as_float(w & 0xffff0000u); }
; __device__ __forceinline__ unsigned pk4_fp8(float a, float b, float c, float d) { unsigned w = 0u; w = __builtin_amdgcn_cvt_pk_fp8_f32(clamp8(a), clamp8(b), w, false); w = __builtin_amdgcn_cvt_pk_fp8_f32(clamp8(c), clamp8(d), w, true); return w; }
;     __device__ __forceinline__ void operator()(const f32x4 (&acc)[2][2][4][2], const Unit& u, int wr, int wc, int fr, int fq) const {
;     ...
;             for (int m = 0; m < 4; ++m) { const size_t r = (size_t)(row0 + ai * HALF + m * 16);
; #pragma unroll
;                 for (int bj = 0; bj < 2; ++bj) { const int col = u.pn * BM + bj * HALF + colw;
;                     const u32x4 gw = *(const u32x4*)(GATE + r * INC + 2 * D + col);
;                     f32x4 r0 = acc[ai][bj][m][0], r1 = acc[ai][bj][m][1];
;                     r0[0] *= bflo(gw.x); r0[1] *= bfhi(gw.x); r0[2] *= bflo(gw.y); r0[3] *= bfhi(gw.y); r1[0] *= bflo(gw.z); r1[1] *= bfhi(gw.z); r1[2] *= bflo(gw.w); r1[3] *= bfhi(gw.w);
;                     u32x2 w; w.x = pk4_fp8(4.f * r0[0], 4.f * r0[1], 4.f * r0[2], 4.f * r0[3]); w.y = pk4_fp8(4.f * r1[0], 4.f * r1[1], 4.f * r1[2], 4.f * r1[3]); *(u32x2*)(MG + r * D + col) = w; }
;                 asm volatile("" ::: "memory"); }
	v_mov_b64_e32 v[8:9], v[48:49]
	v_mov_b64_e32 v[10:11], v[50:51]
	v_lshlrev_b32_e32 v12, 16, v8
	v_and_b32_e32 v8, 0xffff0000, v8
	v_mul_f32_e32 v12, v134, v12
	v_mul_f32_e32 v8, v135, v8
	v_mul_f32_e32 v12, 4.0, v12
	v_mul_f32_e32 v8, 4.0, v8
	v_med3_f32 v12, v12, s33, v229
	v_med3_f32 v18, v8, s33, v229
	v_mov_b32_e32 v8, v65
	v_lshlrev_b32_e32 v13, 16, v9
	v_and_b32_e32 v9, 0xffff0000, v9
	v_cvt_pk_fp8_f32 v8, v12, v18
	v_mul_f32_e32 v13, v136, v13
	v_mul_f32_e32 v9, v137, v9
	v_lshlrev_b32_e32 v16, 16, v10
	v_and_b32_e32 v10, 0xffff0000, v10
	v_mul_f32_e32 v13, 4.0, v13
	v_mul_f32_e32 v9, 4.0, v9
	v_mul_f32_e32 v16, v130, v16
	v_mul_f32_e32 v10, v131, v10
	v_med3_f32 v12, v13, s33, v229
	v_med3_f32 v9, v9, s33, v229
	v_cvt_pk_fp8_f32 v8, v12, v9 op_sel:[0,0,1]
	v_mul_f32_e32 v9, 4.0, v16
	v_mul_f32_e32 v10, 4.0, v10
	v_med3_f32 v13, v9, s33, v229
	v_med3_f32 v10, v10, s33, v229
	v_mov_b32_e32 v9, v65
	v_lshlrev_b32_e32 v17, 16, v11
	v_and_b32_e32 v11, 0xffff0000, v11
	v_cvt_pk_fp8_f32 v9, v13, v10
	v_mul_f32_e32 v17, v132, v17
	v_mul_f32_e32 v11, v133, v11
	v_mul_f32_e32 v12, 4.0, v17
	v_mul_f32_e32 v11, 4.0, v11
	v_med3_f32 v10, v12, s33, v229
	v_med3_f32 v11, v11, s33, v229
	v_cvt_pk_fp8_f32 v9, v10, v11 op_sel:[0,0,1]
	v_add_u32_e32 v52, 0x80, v212
	v_mad_i64_i32 v[52:53], s[6:7], v52, s97, v[2:3]
	v_lshl_add_u64 v[52:53], v[52:53], 0, s[10:11]
	v_lshl_add_u64 v[52:53], v[52:53], 0, v[4:5]
	global_load_dwordx4 v[20:23], v[52:53], off
	global_load_dwordx4 v[24:27], v[52:53], off offset:256
	v_add_u32_e32 v52, 0x90, v212
	v_mad_i64_i32 v[52:53], s[6:7], v52, s97, v[2:3]
	v_lshl_add_u64 v[52:53], v[52:53], 0, s[10:11]
	v_lshl_add_u64 v[52:53], v[52:53], 0, v[4:5]
	global_load_dwordx4 v[28:31], v[52:53], off
	global_load_dwordx4 v[32:35], v[52:53], off offset:256
	v_add_u32_e32 v52, 0xa0, v212
	v_mad_i64_i32 v[52:53], s[6:7], v52, s97, v[2:3]
	v_lshl_add_u64 v[52:53], v[52:53], 0, s[10:11]
	v_lshl_add_u64 v[52:53], v[52:53], 0, v[4:5]
	global_load_dwordx4 v[36:39], v[52:53], off
	global_load_dwordx4 v[40:43], v[52:53], off offset:256
	v_add_u32_e32 v52, 0xb0, v212
	v_mad_i64_i32 v[52:53], s[6:7], v52, s97, v[2:3]
	v_lshl_add_u64 v[52:53], v[52:53], 0, s[10:11]
	v_lshl_add_u64 v[52:53], v[52:53], 0, v[4:5]
	global_load_dwordx4 v[44:47], v[52:53], off
	global_load_dwordx4 v[48:51], v[52:53], off offset:256
	v_add_u32_e32 v10, 0x80, v212
	v_ashrrev_i32_e32 v11, 31, v10
	global_store_dwordx2 v[14:15], v[8:9], off offset:128
	v_lshlrev_b64 v[8:9], 11, v[10:11]
	v_mad_i64_i32 v[10:11], s[6:7], v10, s97, v[2:3]
	v_lshl_add_u64 v[10:11], v[10:11], 0, s[10:11]
	v_lshl_add_u64 v[12:13], v[10:11], 0, v[4:5]
	s_waitcnt vmcnt(8)
	v_mov_b64_e32 v[12:13], v[20:21]
	v_mov_b64_e32 v[14:15], v[22:23]
	v_lshl_add_u64 v[8:9], s[8:9], 0, v[8:9]
	v_lshlrev_b32_e32 v16, 16, v12
	v_and_b32_e32 v12, 0xffff0000, v12
	v_mul_f32_e32 v16, v126, v16
	v_mul_f32_e32 v12, v127, v12
	v_mul_f32_e32 v16, 4.0, v16
	v_mul_f32_e32 v12, 4.0, v12
	v_med3_f32 v16, v16, s33, v229
	v_med3_f32 v20, v12, s33, v229
	v_mov_b32_e32 v12, v65
	v_lshlrev_b32_e32 v17, 16, v13
	v_and_b32_e32 v13, 0xffff0000, v13
	v_cvt_pk_fp8_f32 v12, v16, v20
	v_mul_f32_e32 v17, v128, v17
	v_mul_f32_e32 v13, v129, v13
	v_lshlrev_b32_e32 v18, 16, v14
	v_and_b32_e32 v14, 0xffff0000, v14
	v_mul_f32_e32 v17, 4.0, v17
	v_mul_f32_e32 v13, 4.0, v13
	v_mul_f32_e32 v18, v122, v18
	v_mul_f32_e32 v14, v123, v14
	v_med3_f32 v16, v17, s33, v229
	v_med3_f32 v13, v13, s33, v229
	v_cvt_pk_fp8_f32 v12, v16, v13 op_sel:[0,0,1]
	v_mul_f32_e32 v13, 4.0, v18
	v_mul_f32_e32 v14, 4.0, v14
	v_med3_f32 v17, v13, s33, v229
	v_med3_f32 v14, v14, s33, v229
	v_mov_b32_e32 v13, v65
	v_lshlrev_b32_e32 v19, 16, v15
	v_and_b32_e32 v15, 0xffff0000, v15
	v_cvt_pk_fp8_f32 v13, v17, v14
	v_mul_f32_e32 v19, v124, v19
	v_mul_f32_e32 v15, v125, v15
	v_mul_f32_e32 v16, 4.0, v19
	v_mul_f32_e32 v15, 4.0, v15
	v_med3_f32 v14, v16, s33, v229
	v_med3_f32 v15, v15, s33, v229
	v_cvt_pk_fp8_f32 v13, v14, v15 op_sel:[0,0,1]
	v_lshl_add_u64 v[14:15], v[8:9], 0, v[0:1]
	v_lshl_add_u64 v[8:9], v[10:11], 0, v[6:7]
	global_store_dwordx2 v[14:15], v[12:13], off
	s_waitcnt vmcnt(8)
	v_mov_b64_e32 v[8:9], v[24:25]
	v_mov_b64_e32 v[10:11], v[26:27]
	v_lshlrev_b32_e32 v12, 16, v8
	v_and_b32_e32 v8, 0xffff0000, v8
	v_mul_f32_e32 v12, v118, v12
	v_mul_f32_e32 v8, v119, v8
	v_mul_f32_e32 v12, 4.0, v12
	v_mul_f32_e32 v8, 4.0, v8
	v_med3_f32 v12, v12, s33, v229
	v_med3_f32 v18, v8, s33, v229
	v_mov_b32_e32 v8, v65
	v_lshlrev_b32_e32 v13, 16, v9
	v_and_b32_e32 v9, 0xffff0000, v9
	v_cvt_pk_fp8_f32 v8, v12, v18
	v_mul_f32_e32 v13, v120, v13
	v_mul_f32_e32 v9, v121, v9
	v_lshlrev_b32_e32 v16, 16, v10
	v_and_b32_e32 v10, 0xffff0000, v10
	v_mul_f32_e32 v13, 4.0, v13
	v_mul_f32_e32 v9, 4.0, v9
	v_mul_f32_e32 v16, v114, v16
	v_mul_f32_e32 v10, v115, v10
	v_med3_f32 v12, v13, s33, v229
	v_med3_f32 v9, v9, s33, v229
	v_cvt_pk_fp8_f32 v8, v12, v9 op_sel:[0,0,1]
	v_mul_f32_e32 v9, 4.0, v16
	v_mul_f32_e32 v10, 4.0, v10
	v_med3_f32 v13, v9, s33, v229
	v_med3_f32 v10, v10, s33, v229
	v_mov_b32_e32 v9, v65
	v_lshlrev_b32_e32 v17, 16, v11
	v_and_b32_e32 v11, 0xffff0000, v11
	v_cvt_pk_fp8_f32 v9, v13, v10
	v_mul_f32_e32 v17, v116, v17
	v_mul_f32_e32 v11, v117, v11
	v_mul_f32_e32 v12, 4.0, v17
	v_mul_f32_e32 v11, 4.0, v11
	v_med3_f32 v10, v12, s33, v229
	v_med3_f32 v11, v11, s33, v229
	v_cvt_pk_fp8_f32 v9, v10, v11 op_sel:[0,0,1]
	v_add_u32_e32 v10, 0x90, v212
	v_ashrrev_i32_e32 v11, 31, v10
	global_store_dwordx2 v[14:15], v[8:9], off offset:128
	v_lshlrev_b64 v[8:9], 11, v[10:11]
	v_mad_i64_i32 v[10:11], s[6:7], v10, s97, v[2:3]
	v_lshl_add_u64 v[10:11], v[10:11], 0, s[10:11]
	v_lshl_add_u64 v[12:13], v[10:11], 0, v[4:5]
	s_waitcnt vmcnt(8)
; __device__ __forceinline__ float bflo(unsigned w) { return __uint_as_float(w << 16); }
; __device__ __forceinline__ float bfhi(unsigned w) { return __uint_as_float(w & 0xffff0000u); }
; __device__ __forceinline__ unsigned pk4_fp8(float a, float b, float c, float d) { unsigned w = 0u; w = __builtin_amdgcn_cvt_pk_fp8_f32(clamp8(a), clamp8(b), w, false); w = __builtin_amdgcn_cvt_pk_fp8_f32(clamp8(c), clamp8(d), w, true); return w; }
;     __device__ __forceinline__ void operator()(const f32x4 (&acc)[2][2][4][2], const Unit& u, int wr, int wc, int fr, int fq) const {
;     ...
;             for (int m = 0; m < 4; ++m) { const size_t r = (size_t)(row0 + ai * HALF + m * 16);
; #pragma unroll
;                 for (int bj = 0; bj < 2; ++bj) { const int col = u.pn * BM + bj * HALF + colw;
;                     const u32x4 gw = *(const u32x4*)(GATE + r * INC + 2 * D + col);
;                     f32x4 r0 = acc[ai][bj][m][0], r1 = acc[ai][bj][m][1];
;                     r0[0] *= bflo(gw.x); r0[1] *= bfhi(gw.x); r0[2] *= bflo(gw.y); r0[3] *= bfhi(gw.y); r1[0] *= bflo(gw.z); r1[1] *= bfhi(gw.z); r1[2] *= bflo(gw.w); r1[3] *= bfhi(gw.w);
;                     u32x2 w; w.x = pk4_fp8(4.f * r0[0], 4.f * r0[1], 4.f * r0[2], 4.f * r0[3]); w.y = pk4_fp8(4.f * r1[0], 4.f * r1[1], 4.f * r1[2], 4.f * r1[3]); *(u32x2*)(MG + r * D + col) = w; }
;                 asm volatile("" ::: "memory"); }
	v_mov_b64_e32 v[12:13], v[28:29]
	v_mov_b64_e32 v[14:15], v[30:31]
	v_lshl_add_u64 v[8:9], s[8:9], 0, v[8:9]
	v_lshlrev_b32_e32 v16, 16, v12
	v_and_b32_e32 v12, 0xffff0000, v12
	v_mul_f32_e32 v16, v110, v16
	v_mul_f32_e32 v12, v111, v12
	v_mul_f32_e32 v16, 4.0, v16
	v_mul_f32_e32 v12, 4.0, v12
	v_med3_f32 v16, v16, s33, v229
	v_med3_f32 v20, v12, s33, v229
	v_mov_b32_e32 v12, v65
	v_lshlrev_b32_e32 v17, 16, v13
	v_and_b32_e32 v13, 0xffff0000, v13
	v_cvt_pk_fp8_f32 v12, v16, v20
	v_mul_f32_e32 v17, v112, v17
	v_mul_f32_e32 v13, v113, v13
	v_lshlrev_b32_e32 v18, 16, v14
	v_and_b32_e32 v14, 0xffff0000, v14
	v_mul_f32_e32 v17, 4.0, v17
	v_mul_f32_e32 v13, 4.0, v13
	v_mul_f32_e32 v18, v106, v18
	v_mul_f32_e32 v14, v107, v14
	v_med3_f32 v16, v17, s33, v229
	v_med3_f32 v13, v13, s33, v229
	v_cvt_pk_fp8_f32 v12, v16, v13 op_sel:[0,0,1]
	v_mul_f32_e32 v13, 4.0, v18
	v_mul_f32_e32 v14, 4.0, v14
	v_med3_f32 v17, v13, s33, v229
	v_med3_f32 v14, v14, s33, v229
	v_mov_b32_e32 v13, v65
	v_lshlrev_b32_e32 v19, 16, v15
	v_and_b32_e32 v15, 0xffff0000, v15
	v_cvt_pk_fp8_f32 v13, v17, v14
	v_mul_f32_e32 v19, v108, v19
	v_mul_f32_e32 v15, v109, v15
	v_mul_f32_e32 v16, 4.0, v19
	v_mul_f32_e32 v15, 4.0, v15
	v_med3_f32 v14, v16, s33, v229
	v_med3_f32 v15, v15, s33, v229
	v_cvt_pk_fp8_f32 v13, v14, v15 op_sel:[0,0,1]
	v_lshl_add_u64 v[14:15], v[8:9], 0, v[0:1]
	v_lshl_add_u64 v[8:9], v[10:11], 0, v[6:7]
	global_store_dwordx2 v[14:15], v[12:13], off
	s_waitcnt vmcnt(8)
	v_mov_b64_e32 v[8:9], v[32:33]
	v_mov_b64_e32 v[10:11], v[34:35]
	v_lshlrev_b32_e32 v12, 16, v8
	v_and_b32_e32 v8, 0xffff0000, v8
	v_mul_f32_e32 v12, v102, v12
	v_mul_f32_e32 v8, v103, v8
	v_mul_f32_e32 v12, 4.0, v12
	v_mul_f32_e32 v8, 4.0, v8
	v_med3_f32 v12, v12, s33, v229
	v_med3_f32 v18, v8, s33, v229
	v_mov_b32_e32 v8, v65
	v_lshlrev_b32_e32 v13, 16, v9
	v_and_b32_e32 v9, 0xffff0000, v9
	v_cvt_pk_fp8_f32 v8, v12, v18
	v_mul_f32_e32 v13, v104, v13
	v_mul_f32_e32 v9, v105, v9
	v_lshlrev_b32_e32 v16, 16, v10
	v_and_b32_e32 v10, 0xffff0000, v10
	v_mul_f32_e32 v13, 4.0, v13
	v_mul_f32_e32 v9, 4.0, v9
	v_mul_f32_e32 v16, v98, v16
	v_mul_f32_e32 v10, v99, v10
	v_med3_f32 v12, v13, s33, v229
	v_med3_f32 v9, v9, s33, v229
	v_cvt_pk_fp8_f32 v8, v12, v9 op_sel:[0,0,1]
	v_mul_f32_e32 v9, 4.0, v16
	v_mul_f32_e32 v10, 4.0, v10
	v_med3_f32 v13, v9, s33, v229
	v_med3_f32 v10, v10, s33, v229
	v_mov_b32_e32 v9, v65
	v_lshlrev_b32_e32 v17, 16, v11
	v_and_b32_e32 v11, 0xffff0000, v11
	v_cvt_pk_fp8_f32 v9, v13, v10
	v_mul_f32_e32 v17, v100, v17
	v_mul_f32_e32 v11, v101, v11
	v_mul_f32_e32 v12, 4.0, v17
	v_mul_f32_e32 v11, 4.0, v11
	v_med3_f32 v10, v12, s33, v229
	v_med3_f32 v11, v11, s33, v229
	v_cvt_pk_fp8_f32 v9, v10, v11 op_sel:[0,0,1]
	v_add_u32_e32 v10, 0xa0, v212
	v_ashrrev_i32_e32 v11, 31, v10
	global_store_dwordx2 v[14:15], v[8:9], off offset:128
	v_lshlrev_b64 v[8:9], 11, v[10:11]
	v_mad_i64_i32 v[10:11], s[6:7], v10, s97, v[2:3]
	v_lshl_add_u64 v[10:11], v[10:11], 0, s[10:11]
	v_lshl_add_u64 v[12:13], v[10:11], 0, v[4:5]
	s_waitcnt vmcnt(8)
	v_mov_b64_e32 v[12:13], v[36:37]
	v_mov_b64_e32 v[14:15], v[38:39]
	v_lshl_add_u64 v[8:9], s[8:9], 0, v[8:9]
	v_lshlrev_b32_e32 v16, 16, v12
	v_and_b32_e32 v12, 0xffff0000, v12
	v_mul_f32_e32 v16, v94, v16
	v_mul_f32_e32 v12, v95, v12
	v_mul_f32_e32 v16, 4.0, v16
	v_mul_f32_e32 v12, 4.0, v12
	v_med3_f32 v16, v16, s33, v229
	v_med3_f32 v20, v12, s33, v229
	v_mov_b32_e32 v12, v65
	v_lshlrev_b32_e32 v17, 16, v13
	v_and_b32_e32 v13, 0xffff0000, v13
	v_cvt_pk_fp8_f32 v12, v16, v20
	v_mul_f32_e32 v17, v96, v17
	v_mul_f32_e32 v13, v97, v13
	v_lshlrev_b32_e32 v18, 16, v14
	v_and_b32_e32 v14, 0xffff0000, v14
	v_mul_f32_e32 v17, 4.0, v17
	v_mul_f32_e32 v13, 4.0, v13
	v_mul_f32_e32 v18, v90, v18
	v_mul_f32_e32 v14, v91, v14
	v_med3_f32 v16, v17, s33, v229
	v_med3_f32 v13, v13, s33, v229
	v_cvt_pk_fp8_f32 v12, v16, v13 op_sel:[0,0,1]
	v_mul_f32_e32 v13, 4.0, v18
	v_mul_f32_e32 v14, 4.0, v14
	v_med3_f32 v17, v13, s33, v229
	v_med3_f32 v14, v14, s33, v229
	v_mov_b32_e32 v13, v65
	v_lshlrev_b32_e32 v19, 16, v15
	v_and_b32_e32 v15, 0xffff0000, v15
	v_cvt_pk_fp8_f32 v13, v17, v14
	v_mul_f32_e32 v19, v92, v19
	v_mul_f32_e32 v15, v93, v15
	v_mul_f32_e32 v16, 4.0, v19
	v_mul_f32_e32 v15, 4.0, v15
	v_med3_f32 v14, v16, s33, v229
	v_med3_f32 v15, v15, s33, v229
	v_cvt_pk_fp8_f32 v13, v14, v15 op_sel:[0,0,1]
	v_lshl_add_u64 v[14:15], v[8:9], 0, v[0:1]
	v_lshl_add_u64 v[8:9], v[10:11], 0, v[6:7]
	global_store_dwordx2 v[14:15], v[12:13], off
	s_waitcnt vmcnt(8)
; __device__ __forceinline__ float bflo(unsigned w) { return __uint_as_float(w << 16); }
; __device__ __forceinline__ float bfhi(unsigned w) { return __uint_as_float(w & 0xffff0000u); }
; __device__ __forceinline__ unsigned pk4_fp8(float a, float b, float c, float d) { unsigned w = 0u; w = __builtin_amdgcn_cvt_pk_fp8_f32(clamp8(a), clamp8(b), w, false); w = __builtin_amdgcn_cvt_pk_fp8_f32(clamp8(c), clamp8(d), w, true); return w; }
;     __device__ __forceinline__ void operator()(const f32x4 (&acc)[2][2][4][2], const Unit& u, int wr, int wc, int fr, int fq) const {
;     ...
;             for (int m = 0; m < 4; ++m) { const size_t r = (size_t)(row0 + ai * HALF + m * 16);
; #pragma unroll
;                 for (int bj = 0; bj < 2; ++bj) { const int col = u.pn * BM + bj * HALF + colw;
;                     const u32x4 gw = *(const u32x4*)(GATE + r * INC + 2 * D + col);
;                     f32x4 r0 = acc[ai][bj][m][0], r1 = acc[ai][bj][m][1];
;                     r0[0] *= bflo(gw.x); r0[1] *= bfhi(gw.x); r0[2] *= bflo(gw.y); r0[3] *= bfhi(gw.y); r1[0] *= bflo(gw.z); r1[1] *= bfhi(gw.z); r1[2] *= bflo(gw.w); r1[3] *= bfhi(gw.w);
;                     u32x2 w; w.x = pk4_fp8(4.f * r0[0], 4.f * r0[1], 4.f * r0[2], 4.f * r0[3]); w.y = pk4_fp8(4.f * r1[0], 4.f * r1[1], 4.f * r1[2], 4.f * r1[3]); *(u32x2*)(MG + r * D + col) = w; }
;                 asm volatile("" ::: "memory"); }
	v_mov_b64_e32 v[8:9], v[40:41]
	v_mov_b64_e32 v[10:11], v[42:43]
	v_lshlrev_b32_e32 v12, 16, v8
	v_and_b32_e32 v8, 0xffff0000, v8
	v_mul_f32_e32 v12, v86, v12
	v_mul_f32_e32 v8, v87, v8
	v_mul_f32_e32 v12, 4.0, v12
	v_mul_f32_e32 v8, 4.0, v8
	v_med3_f32 v12, v12, s33, v229
	v_med3_f32 v18, v8, s33, v229
	v_mov_b32_e32 v8, v65
	v_lshlrev_b32_e32 v13, 16, v9
	v_and_b32_e32 v9, 0xffff0000, v9
	v_cvt_pk_fp8_f32 v8, v12, v18
	v_mul_f32_e32 v13, v88, v13
	v_mul_f32_e32 v9, v89, v9
	v_lshlrev_b32_e32 v16, 16, v10
	v_and_b32_e32 v10, 0xffff0000, v10
	v_mul_f32_e32 v13, 4.0, v13
	v_mul_f32_e32 v9, 4.0, v9
	v_mul_f32_e32 v16, v82, v16
	v_mul_f32_e32 v10, v83, v10
	v_med3_f32 v12, v13, s33, v229
	v_med3_f32 v9, v9, s33, v229
	v_cvt_pk_fp8_f32 v8, v12, v9 op_sel:[0,0,1]
	v_mul_f32_e32 v9, 4.0, v16
	v_mul_f32_e32 v10, 4.0, v10
	v_med3_f32 v13, v9, s33, v229
	v_med3_f32 v10, v10, s33, v229
	v_mov_b32_e32 v9, v65
	v_lshlrev_b32_e32 v17, 16, v11
	v_and_b32_e32 v11, 0xffff0000, v11
	v_cvt_pk_fp8_f32 v9, v13, v10
	v_mul_f32_e32 v17, v84, v17
	v_mul_f32_e32 v11, v85, v11
	v_mul_f32_e32 v12, 4.0, v17
	v_mul_f32_e32 v11, 4.0, v11
	v_med3_f32 v10, v12, s33, v229
	v_med3_f32 v11, v11, s33, v229
	v_cvt_pk_fp8_f32 v9, v10, v11 op_sel:[0,0,1]
	v_add_u32_e32 v10, 0xb0, v212
	v_mad_i64_i32 v[2:3], s[6:7], v10, s97, v[2:3]
	global_store_dwordx2 v[14:15], v[8:9], off offset:128
	v_lshl_add_u64 v[2:3], v[2:3], 0, s[10:11]
	v_ashrrev_i32_e32 v11, 31, v10
	v_lshl_add_u64 v[4:5], v[2:3], 0, v[4:5]
	v_lshlrev_b64 v[8:9], 11, v[10:11]
	s_waitcnt vmcnt(8)
	v_mov_b64_e32 v[10:11], v[44:45]
	v_mov_b64_e32 v[12:13], v[46:47]
	v_lshl_add_u64 v[8:9], s[8:9], 0, v[8:9]
	v_lshl_add_u64 v[0:1], v[8:9], 0, v[0:1]
	v_lshl_add_u64 v[2:3], v[2:3], 0, v[6:7]
	s_mov_b64 s[8:9], -1
	v_lshlrev_b32_e32 v4, 16, v10
	v_and_b32_e32 v5, 0xffff0000, v10
	v_mul_f32_e32 v4, v78, v4
	v_mul_f32_e32 v5, v79, v5
	v_mul_f32_e32 v4, 4.0, v4
	v_mul_f32_e32 v5, 4.0, v5
	v_med3_f32 v16, v4, s33, v229
	v_med3_f32 v5, v5, s33, v229
	v_mov_b32_e32 v4, v65
	v_lshlrev_b32_e32 v10, 16, v11
	v_and_b32_e32 v11, 0xffff0000, v11
	v_cvt_pk_fp8_f32 v4, v16, v5
	v_mul_f32_e32 v10, v80, v10
	v_mul_f32_e32 v11, v81, v11
	v_lshlrev_b32_e32 v14, 16, v12
	v_and_b32_e32 v12, 0xffff0000, v12
	v_mul_f32_e32 v10, 4.0, v10
	v_mul_f32_e32 v11, 4.0, v11
	v_mul_f32_e32 v14, v74, v14
	v_mul_f32_e32 v12, v75, v12
	v_lshlrev_b32_e32 v15, 16, v13
	v_and_b32_e32 v13, 0xffff0000, v13
	v_med3_f32 v5, v10, s33, v229
	v_med3_f32 v10, v11, s33, v229
	v_mul_f32_e32 v13, v77, v13
	v_cvt_pk_fp8_f32 v4, v5, v10 op_sel:[0,0,1]
	v_mul_f32_e32 v5, 4.0, v14
	v_mul_f32_e32 v10, 4.0, v12
	v_mul_f32_e32 v12, 4.0, v13
	v_med3_f32 v13, v5, s33, v229
	v_med3_f32 v10, v10, s33, v229
	v_mov_b32_e32 v5, v65
	v_cvt_pk_fp8_f32 v5, v13, v10
	v_mul_f32_e32 v15, v76, v15
	v_mul_f32_e32 v11, 4.0, v15
	v_med3_f32 v10, v11, s33, v229
	v_med3_f32 v11, v12, s33, v229
	v_cvt_pk_fp8_f32 v5, v10, v11 op_sel:[0,0,1]
	global_store_dwordx2 v[0:1], v[4:5], off
	s_waitcnt vmcnt(8)
	v_mov_b64_e32 v[2:3], v[48:49]
	v_mov_b64_e32 v[4:5], v[50:51]
	v_lshlrev_b32_e32 v6, 16, v2
	v_and_b32_e32 v2, 0xffff0000, v2
	v_mul_f32_e32 v6, v70, v6
	v_mul_f32_e32 v2, v71, v2
	v_mul_f32_e32 v6, 4.0, v6
	v_mul_f32_e32 v2, 4.0, v2
	v_med3_f32 v6, v6, s33, v229
	v_med3_f32 v10, v2, s33, v229
	v_mov_b32_e32 v2, v65
	v_lshlrev_b32_e32 v7, 16, v3
	v_and_b32_e32 v3, 0xffff0000, v3
	v_cvt_pk_fp8_f32 v2, v6, v10
	v_mul_f32_e32 v7, v72, v7
	v_mul_f32_e32 v3, v73, v3
	v_lshlrev_b32_e32 v8, 16, v4
	v_and_b32_e32 v4, 0xffff0000, v4
	v_mul_f32_e32 v7, 4.0, v7
	v_mul_f32_e32 v3, 4.0, v3
	v_mul_f32_e32 v8, v66, v8
	v_mul_f32_e32 v4, v67, v4
	v_med3_f32 v6, v7, s33, v229
	v_med3_f32 v3, v3, s33, v229
	v_cvt_pk_fp8_f32 v2, v6, v3 op_sel:[0,0,1]
	v_mul_f32_e32 v3, 4.0, v8
	v_mul_f32_e32 v4, 4.0, v4
	v_med3_f32 v7, v3, s33, v229
	v_med3_f32 v4, v4, s33, v229
	v_mov_b32_e32 v3, v65
	v_lshlrev_b32_e32 v9, 16, v5
	v_and_b32_e32 v5, 0xffff0000, v5
	v_cvt_pk_fp8_f32 v3, v7, v4
	v_mul_f32_e32 v9, v68, v9
	v_mul_f32_e32 v5, v69, v5
	v_mul_f32_e32 v6, 4.0, v9
	v_mul_f32_e32 v5, 4.0, v5
	v_med3_f32 v4, v6, s33, v229
	v_med3_f32 v5, v5, s33, v229
	v_cvt_pk_fp8_f32 v3, v4, v5 op_sel:[0,0,1]
	global_store_dwordx2 v[0:1], v[2:3], off offset:128
	s_cbranch_vccnz .LBB0_691
	s_and_b64 vcc, exec, s[40:41]
	s_cbranch_vccnz .LBB0_690
	s_barrier
	s_branch .LBB0_690

; template <bool last> __device__ __forceinline__ void combine_ln2_row(const Params& p, int l, int t, const LAS MoeTab* tb, int lane, bool dry = false) {
;     ...
;     { const int s = lane & 15;
;       if (s < 8) { const int e = ((const int*)(p.ws + WS_TOPE))[t * 8 + s]; row_l = tb->rb[e] + ((const int*)(p.ws + WS_TOPPOS))[t * 8 + s]; w_l = ((const float*)(p.ws + WS_TOPW))[t * 8 + s]; }
;       else { row_l = tb->rb[64] + t; w_l = 1.0f; } }
.LBB0_1511:
	s_or_saveexec_b64 s[0:1], s[0:1]
	v_mov_b32_e32 v21, 1.0
	s_xor_b64 exec, exec, s[0:1]
	s_cbranch_execz .LBB0_1513
	v_add_u32_e32 v2, s31, v1
	v_ashrrev_i32_e32 v3, 31, v2
	v_readlane_b32 s10, v251, 9
	v_lshlrev_b64 v[2:3], 2, v[2:3]
	v_readlane_b32 s11, v251, 10
	s_nop 1
	v_lshl_add_u64 v[4:5], s[10:11], 0, v[2:3]
	global_load_dword v1, v[4:5], off
	v_readlane_b32 s10, v251, 11
	v_readlane_b32 s11, v251, 12
	s_nop 1
	v_lshl_add_u64 v[4:5], s[10:11], 0, v[2:3]
	v_readlane_b32 s10, v251, 13
	v_readlane_b32 s11, v251, 14
	global_load_dword v4, v[4:5], off
	s_nop 0
	v_lshl_add_u64 v[2:3], s[10:11], 0, v[2:3]
	global_load_dword v21, v[2:3], off
	s_waitcnt vmcnt(2)
	v_lshl_add_u32 v1, v1, 2, 0
	v_add_u32_e32 v1, 0x23104, v1
	ds_read_b32 v1, v1
	s_waitcnt vmcnt(0) lgkmcnt(0)
	v_add_u32_e32 v19, v4, v1

; template <bool last> __device__ __forceinline__ void combine_ln2_row(const Params& p, int l, int t, const LAS MoeTab* tb, int lane, bool dry = false) {
;     ...
;     { const int s = lane & 15;
;       if (s < 8) { const int e = ((const int*)(p.ws + WS_TOPE))[t * 8 + s]; row_l = tb->rb[e] + ((const int*)(p.ws + WS_TOPPOS))[t * 8 + s]; w_l = ((const float*)(p.ws + WS_TOPW))[t * 8 + s]; }
;       else { row_l = tb->rb[64] + t; w_l = 1.0f; } }
.LBB0_1519:
	s_or_saveexec_b64 s[0:1], s[0:1]
	v_mov_b32_e32 v22, 1.0
	s_xor_b64 exec, exec, s[0:1]
	s_cbranch_execz .LBB0_1521
	v_add_u32_e32 v2, s31, v1
	v_ashrrev_i32_e32 v3, 31, v2
	v_readlane_b32 s10, v251, 9
	v_lshlrev_b64 v[2:3], 2, v[2:3]
	v_readlane_b32 s11, v251, 10
	s_nop 1
	v_lshl_add_u64 v[4:5], s[10:11], 0, v[2:3]
	global_load_dword v1, v[4:5], off
	v_readlane_b32 s10, v251, 11
	v_readlane_b32 s11, v251, 12
	s_nop 1
	v_lshl_add_u64 v[4:5], s[10:11], 0, v[2:3]
	v_readlane_b32 s10, v251, 13
	v_readlane_b32 s11, v251, 14
	global_load_dword v4, v[4:5], off
	s_nop 0
	v_lshl_add_u64 v[2:3], s[10:11], 0, v[2:3]
	global_load_dword v22, v[2:3], off
	s_waitcnt vmcnt(2)
	v_lshl_add_u32 v1, v1, 2, 0
	v_add_u32_e32 v1, 0x23104, v1
	ds_read_b32 v1, v1
	s_waitcnt vmcnt(0) lgkmcnt(0)
	v_add_u32_e32 v19, v4, v1
